# moe_stagger step 48 (8 groups x ~1.3us)
# speedup vs baseline: 1.0005x; 1.0005x over previous
.Lstg_loop:
	s_sleep 48
	s_add_i32 s98, s98, -1
	s_cmp_lg_u32 s98, 0
	s_cbranch_scc1 .Lstg_loop
